# P5 (mLSTM finalize): wave-invariant norm-weight load hoisted out of loop, join waits counted (vmcnt 5) so the next-item prefetch stays in flight; plus P7 row-pass pipelining and batched DOWN epilogue
# speedup vs baseline: 1.0227x; 1.0135x over previous
; #define P5_LOAD(nv_, den_, mt_, mo_, it_) do { const int t_ = (it_) >> 2, hh_ = (it_) & 3; nv_ = *(const f32x4*)(NUM + (size_t)t_ * MW + hh_ * 256 + 4 * lane); \
;         den_ = DEN[(size_t)hh_ * T + t_]; mt_ = GM[(size_t)hh_ * T + t_]; mo_ = *(const v2u*)(MO + (size_t)t_ * MW + hh_ * 256 + 4 * lane); } while (0)
; __device__ __forceinline__ void mlstm_norm_phase(const Args& a, int lane, int wave) {
;     ...
;     int it = gw; const int NIT = T * 4;
;     if (it < NIT) P5_LOAD(nva, dena, mta, moa, it);
.LBB0_875:
	s_cmp_lt_i32 s92, 6
	s_cselect_b64 s[0:1], -1, 0
	s_and_b64 s[8:9], s[0:1], s[6:7]
	s_andn2_b64 vcc, exec, s[8:9]
	s_cbranch_vccnz .LBB0_885
	s_lshl_b32 s0, s74, 3
	s_add_i32 s23, s94, s0
	s_cmpk_gt_i32 s23, 0x7fff
	s_cbranch_scc1 .LBB0_885
	s_add_u32 s2, s58, 0x6b0000
	s_load_dword s20, s[96:97], 0xc8
	s_addc_u32 s3, s59, 0
	s_add_u32 s12, s58, 0x680000
	s_addc_u32 s13, s59, 0
	s_add_u32 s14, s58, 0xe800000
	s_addc_u32 s15, s59, 0
	s_waitcnt lgkmcnt(0)
	s_lshl_b32 s16, s20, 3
	s_add_u32 s21, s58, 0x9800000
	s_addc_u32 s22, s59, 0
	s_add_u32 s24, s58, 0xc800000
	s_addc_u32 s25, s59, 0
	s_ashr_i32 s0, s23, 2
	v_readlane_b32 s1, v244, 0
	s_bfe_u32 s26, s1, 0x20006
	s_ashr_i32 s1, s0, 31
	s_lshl_b64 s[6:7], s[0:1], 12
	s_add_u32 s6, s24, s6
	s_addc_u32 s7, s25, s7
	s_lshl_b32 s27, s26, 10
	s_add_u32 s6, s6, s27
	s_addc_u32 s7, s7, 0
	s_lshl_b32 s17, s26, 13
	s_add_u32 s10, s17, s0
	s_addc_u32 s11, 0, s1
	s_lshl_b64 s[10:11], s[10:11], 2
	s_add_u32 s18, s2, s10
	s_addc_u32 s19, s3, s11
	s_add_u32 s10, s12, s10
	s_addc_u32 s11, s13, s11
	s_lshl_b64 s[0:1], s[0:1], 11
	v_mov_b32_e32 v11, 0
	s_add_u32 s0, s21, s0
	global_load_dword v1, v11, s[18:19]
	global_load_dword v24, v11, s[10:11]
	s_addc_u32 s1, s22, s1
	s_lshl_b32 s10, s26, 9
	v_lshlrev_b32_e32 v10, 4, v175
	s_add_u32 s0, s0, s10
	s_addc_u32 s1, s1, 0
	v_lshlrev_b32_e32 v6, 3, v175
	global_load_dwordx4 v[2:5], v10, s[6:7]
	global_load_dwordx2 v[12:13], v6, s[0:1]
	v_mbcnt_lo_u32_b32 v9, -1, 0
	v_mbcnt_hi_u32_b32 v9, -1, v9
	v_and_b32_e32 v14, 64, v9
	v_add_u32_e32 v14, 64, v14
	v_xor_b32_e32 v15, 1, v9
	v_cmp_lt_i32_e32 vcc, v15, v14
	s_add_u32 s0, s24, s27
	s_addc_u32 s1, s25, 0
	v_cndmask_b32_e32 v15, v9, v15, vcc
	v_lshlrev_b32_e32 v25, 2, v15
	v_xor_b32_e32 v15, 2, v9
	v_cmp_lt_i32_e32 vcc, v15, v14
	v_lshl_add_u64 v[16:17], s[0:1], 0, v[10:11]
	s_add_u32 s0, s21, s10
	v_cndmask_b32_e32 v15, v9, v15, vcc
	v_lshlrev_b32_e32 v26, 2, v15
	v_xor_b32_e32 v15, 4, v9
	v_cmp_lt_i32_e32 vcc, v15, v14
	v_mov_b32_e32 v7, v11
	s_addc_u32 s1, s22, 0
	v_cndmask_b32_e32 v15, v9, v15, vcc
	v_lshlrev_b32_e32 v27, 2, v15
	v_xor_b32_e32 v15, 8, v9
	v_cmp_lt_i32_e32 vcc, v15, v14
	v_lshlrev_b32_e32 v8, 2, v175
	v_lshl_add_u64 v[18:19], s[0:1], 0, v[6:7]
	v_cndmask_b32_e32 v15, v9, v15, vcc
	v_lshlrev_b32_e32 v28, 2, v15
	v_xor_b32_e32 v15, 16, v9
	v_cmp_lt_i32_e32 vcc, v15, v14
	s_lshl_b32 s0, s74, 11
	s_lshl_b32 s1, s94, 8
	v_cndmask_b32_e32 v15, v9, v15, vcc
	v_lshlrev_b32_e32 v29, 2, v15
	v_xor_b32_e32 v15, 32, v9
	v_cmp_lt_i32_e32 vcc, v15, v14
	s_mov_b32 s11, 0
	s_add_i32 s18, s0, s1
	v_cndmask_b32_e32 v9, v9, v15, vcc
	v_lshlrev_b32_e32 v30, 2, v9
	v_lshl_add_u64 v[14:15], s[86:87], 0, v[10:11]
	s_lshl_b32 s19, s20, 12
	s_lshl_b32 s20, s20, 4
	v_mov_b32_e32 v10, 0x358637bd
	s_mov_b32 s21, 0xf800000
	v_mov_b32_e32 v31, 0x260
	v_lshlrev_b32_e32 v32, 1, v8
	s_and_b32 s24, s18, 0x300
	s_lshl_b32 s10, s24, 2
	v_lshl_add_u64 v[22:23], v[14:15], 0, s[10:11]
	global_load_dwordx4 v[240:243], v[22:23], off
	s_waitcnt vmcnt(0)
	s_branch .LBB0_880

.Lp5_gob:
	v_mul_f32_e32 v35, 0xbfb8aa3b, v34
	v_exp_f32_e32 v35, v35
	v_max_f32_e64 v36, |v33|, |v33|
	v_max_f32_e32 v35, v36, v35
	v_div_scale_f32 v36, s[0:1], v35, v35, v7
	v_rcp_f32_e32 v37, v36
	v_div_scale_f32 v38, vcc, v7, v35, v7
	v_div_scale_f32 v39, s[0:1], v35, v35, v6
	v_fma_f32 v40, -v36, v37, 1.0
	v_fmac_f32_e32 v37, v40, v37
	v_mul_f32_e32 v40, v38, v37
	v_fma_f32 v41, -v36, v40, v38
	v_fmac_f32_e32 v40, v41, v37
	v_fma_f32 v36, -v36, v40, v38
	v_rcp_f32_e32 v38, v39
	v_div_fmas_f32 v36, v36, v37, v40
	v_div_fixup_f32 v41, v36, v35, v7
	v_fma_f32 v36, -v39, v38, 1.0
	v_fmac_f32_e32 v38, v36, v38
	v_div_scale_f32 v36, vcc, v6, v35, v6
	v_mul_f32_e32 v37, v36, v38
	v_fma_f32 v40, -v39, v37, v36
	v_fmac_f32_e32 v37, v40, v38
	v_fma_f32 v36, -v39, v37, v36
	v_div_scale_f32 v39, s[0:1], v35, v35, v9
	v_rcp_f32_e32 v42, v39
	v_div_fmas_f32 v36, v36, v38, v37
	v_div_fixup_f32 v40, v36, v35, v6
	v_fma_f32 v36, -v39, v42, 1.0
	v_fmac_f32_e32 v42, v36, v42
	v_div_scale_f32 v36, vcc, v9, v35, v9
	v_mul_f32_e32 v37, v36, v42
	v_fma_f32 v38, -v39, v37, v36
	v_fmac_f32_e32 v37, v38, v42
	v_div_scale_f32 v38, s[0:1], v35, v35, v8
	v_fma_f32 v36, -v39, v37, v36
	v_rcp_f32_e32 v39, v38
	v_div_fmas_f32 v36, v36, v42, v37
	v_div_fixup_f32 v43, v36, v35, v9
	v_fma_f32 v36, -v38, v39, 1.0
	v_fmac_f32_e32 v39, v36, v39
	v_div_scale_f32 v36, vcc, v8, v35, v8
	v_mul_f32_e32 v37, v36, v39
	v_fma_f32 v42, -v38, v37, v36
	v_fmac_f32_e32 v37, v42, v39
	v_fma_f32 v36, -v38, v37, v36
	v_div_fmas_f32 v36, v36, v39, v37
	v_div_fixup_f32 v42, v36, v35, v8
	v_pk_mul_f32 v[36:37], v[42:43], v[42:43]
	v_pk_mul_f32 v[38:39], v[40:41], v[40:41]
	s_nop 0
	v_pk_mov_b32 v[44:45], v[38:39], v[36:37] op_sel:[1,0]
	v_mov_b32_e32 v39, v37
	v_pk_add_f32 v[36:37], v[44:45], v[38:39]
	s_nop 0
	v_add_f32_e32 v35, v36, v37
	ds_bpermute_b32 v36, v25, v35
	s_waitcnt lgkmcnt(0)
	v_add_f32_e32 v35, v35, v36
	ds_bpermute_b32 v44, v26, v35
	s_waitcnt lgkmcnt(0)
	v_add_f32_e32 v22, v35, v44
	ds_bpermute_b32 v23, v27, v22
	s_waitcnt lgkmcnt(0)
	v_add_f32_e32 v22, v22, v23
	ds_bpermute_b32 v23, v28, v22
	s_waitcnt lgkmcnt(0)
	v_add_f32_e32 v22, v22, v23
	ds_bpermute_b32 v23, v29, v22
	s_waitcnt lgkmcnt(0)
	v_add_f32_e32 v22, v22, v23
	ds_bpermute_b32 v23, v30, v22
	s_waitcnt lgkmcnt(0)
	v_add_f32_e32 v22, v22, v23
	v_fmamk_f32 v22, v22, 0x3b800000, v10
	v_mul_f32_e32 v23, 0x4f800000, v22
	v_cmp_gt_f32_e32 vcc, s21, v22
	s_nop 1
	v_cndmask_b32_e32 v22, v22, v23, vcc
	v_sqrt_f32_e32 v23, v22
	s_nop 0
	v_add_u32_e32 v35, -1, v23
	v_fma_f32 v44, -v35, v23, v22
	v_cmp_ge_f32_e64 s[6:7], 0, v44
	v_add_u32_e32 v44, 1, v23
	s_nop 0
	v_cndmask_b32_e64 v35, v23, v35, s[6:7]
	v_fma_f32 v23, -v44, v23, v22
	v_cmp_lt_f32_e64 s[6:7], 0, v23
	s_nop 1
	v_cndmask_b32_e64 v23, v35, v44, s[6:7]
	v_mul_f32_e32 v35, 0x37800000, v23
	v_cndmask_b32_e32 v23, v23, v35, vcc
	v_cmp_class_f32_e32 vcc, v22, v31
	s_nop 1
	v_cndmask_b32_e32 v22, v23, v22, vcc
	v_div_scale_f32 v23, s[0:1], v22, v22, 1.0
	v_rcp_f32_e32 v35, v23
	s_ashr_i32 s0, s22, 2
	s_ashr_i32 s1, s0, 31
	s_lshl_b64 s[0:1], s[0:1], 12
	v_fma_f32 v44, -v23, v35, 1.0
	v_fmac_f32_e32 v35, v44, v35
	v_div_scale_f32 v44, vcc, 1.0, v22, 1.0
	v_mul_f32_e32 v45, v44, v35
	v_fma_f32 v46, -v23, v45, v44
	v_fmac_f32_e32 v45, v46, v35
	v_fma_f32 v23, -v23, v45, v44
	v_div_fmas_f32 v23, v23, v35, v45
	v_lshlrev_b32_e32 v35, 16, v20
	v_mul_f32_e32 v35, 0xbfb8aa3b, v35
	v_and_b32_e32 v44, 0xffff0000, v20
	v_exp_f32_e32 v35, v35
	v_mul_f32_e32 v44, 0xbfb8aa3b, v44
	v_exp_f32_e32 v45, v44
	v_div_fixup_f32 v22, v23, v22, 1.0
	v_add_f32_e32 v23, 1.0, v35
	v_rcp_f32_e32 v44, v23
	v_add_f32_e32 v23, 1.0, v45
	v_rcp_f32_e32 v45, v23
	v_pk_mul_f32 v[40:41], v[40:41], v[22:23] op_sel_hi:[1,0]
	v_lshlrev_b32_e32 v23, 16, v21
	v_mul_f32_e32 v23, 0xbfb8aa3b, v23
	v_and_b32_e32 v35, 0xffff0000, v21
	v_exp_f32_e32 v23, v23
	v_mul_f32_e32 v35, 0xbfb8aa3b, v35
	v_exp_f32_e32 v35, v35
	v_pk_mul_f32 v[36:37], v[240:241], v[40:41]
	v_add_f32_e32 v23, 1.0, v23
	v_rcp_f32_e32 v40, v23
	v_add_f32_e32 v23, 1.0, v35
	v_rcp_f32_e32 v41, v23
	v_pk_mul_f32 v[22:23], v[42:43], v[22:23] op_sel_hi:[1,0]
	s_add_u32 s0, s14, s0
	v_pk_mul_f32 v[22:23], v[242:243], v[22:23]
	s_addc_u32 s1, s15, s1
	v_pk_mul_f32 v[36:37], v[44:45], v[36:37]
	v_pk_mul_f32 v[22:23], v[40:41], v[22:23]
	s_add_u32 s0, s0, s10
	v_cvt_pk_bf16_f32 v36, v36, v37
	v_cvt_pk_bf16_f32 v37, v22, v23
	s_addc_u32 s1, s1, 0
	global_store_dwordx2 v32, v[36:37], s[0:1] offset:2048

; #define P5_LOAD(nv_, den_, mt_, mo_, it_) do { const int t_ = (it_) >> 2, hh_ = (it_) & 3; nv_ = *(const f32x4*)(NUM + (size_t)t_ * MW + hh_ * 256 + 4 * lane); \
;         den_ = DEN[(size_t)hh_ * T + t_]; mt_ = GM[(size_t)hh_ * T + t_]; mo_ = *(const v2u*)(MO + (size_t)t_ * MW + hh_ * 256 + 4 * lane); } while (0)
; __device__ __forceinline__ void mlstm_norm_phase(const Args& a, int lane, int wave) {
;     ...
;     for (; it < NIT; it += 2 * NGW) {
;         const int i2 = it + NGW, i3 = it + 2 * NGW;
;         if (i2 < NIT) P5_LOAD(nvb, denb, mtb, mob, i2);
;         P5_ITEM(nva, dena, mta, moa, it);
.LBB0_880:
	s_add_i32 s22, s23, s16
	s_cmp_lt_i32 s22, 0x8000
	s_cselect_b64 s[0:1], -1, 0
	s_cmpk_gt_i32 s22, 0x7fff
	s_cbranch_scc1 .LBB0_882
	s_ashr_i32 s6, s22, 2
	s_ashr_i32 s7, s6, 31
	s_lshl_b64 s[24:25], s[6:7], 12
	v_lshl_add_u64 v[6:7], v[16:17], 0, s[24:25]
	s_add_u32 s24, s6, s17
	s_addc_u32 s25, s7, 0
	s_lshl_b64 s[24:25], s[24:25], 2
	s_add_u32 s26, s2, s24
	s_addc_u32 s27, s3, s25
	s_add_u32 s24, s12, s24
	s_addc_u32 s25, s13, s25
	s_lshl_b64 s[6:7], s[6:7], 11
	v_lshl_add_u64 v[20:21], v[18:19], 0, s[6:7]
	global_load_dword v33, v11, s[26:27]
	global_load_dword v34, v11, s[24:25]
	s_nop 0
	global_load_dwordx4 v[6:9], v[6:7], off
	s_nop 0
	global_load_dwordx2 v[20:21], v[20:21], off
	s_waitcnt vmcnt(5)
	s_branch .Lp5_goa

; #define P5_LOAD(nv_, den_, mt_, mo_, it_) do { const int t_ = (it_) >> 2, hh_ = (it_) & 3; nv_ = *(const f32x4*)(NUM + (size_t)t_ * MW + hh_ * 256 + 4 * lane); \
;         den_ = DEN[(size_t)hh_ * T + t_]; mt_ = GM[(size_t)hh_ * T + t_]; mo_ = *(const v2u*)(MO + (size_t)t_ * MW + hh_ * 256 + 4 * lane); } while (0)
; __device__ __forceinline__ void mlstm_norm_phase(const Args& a, int lane, int wave) {
;     ...
;     for (; it < NIT; it += 2 * NGW) {
;         const int i2 = it + NGW, i3 = it + 2 * NGW;
;         if (i2 < NIT) P5_LOAD(nvb, denb, mtb, mob, i2);
;         P5_ITEM(nva, dena, mta, moa, it);
;         if (i2 < NIT) { if (i3 < NIT) P5_LOAD(nva, dena, mta, moa, i3); P5_ITEM(nvb, denb, mtb, mob, i2); }
.Lp5_goa:
	v_mul_f32_e32 v22, 0xbfb8aa3b, v24
	v_exp_f32_e32 v22, v22
	v_max_f32_e64 v23, |v1|, |v1|
	s_and_b32 s24, s18, 0x300
	s_lshl_b32 s10, s24, 2
	v_max_f32_e32 v22, v23, v22
	v_div_scale_f32 v23, s[6:7], v22, v22, v3
	v_rcp_f32_e32 v35, v23
	v_div_scale_f32 v36, vcc, v3, v22, v3
	v_div_scale_f32 v37, s[6:7], v22, v22, v2
	v_fma_f32 v38, -v23, v35, 1.0
	v_fmac_f32_e32 v35, v38, v35
	v_mul_f32_e32 v38, v36, v35
	v_fma_f32 v39, -v23, v38, v36
	v_fmac_f32_e32 v38, v39, v35
	v_fma_f32 v23, -v23, v38, v36
	v_rcp_f32_e32 v36, v37
	v_div_fmas_f32 v23, v23, v35, v38
	v_div_fixup_f32 v41, v23, v22, v3
	v_fma_f32 v23, -v37, v36, 1.0
	v_fmac_f32_e32 v36, v23, v36
	v_div_scale_f32 v23, vcc, v2, v22, v2
	v_mul_f32_e32 v35, v23, v36
	v_fma_f32 v38, -v37, v35, v23
	v_fmac_f32_e32 v35, v38, v36
	v_fma_f32 v23, -v37, v35, v23
	v_div_scale_f32 v37, s[6:7], v22, v22, v5
	v_rcp_f32_e32 v38, v37
	v_div_fmas_f32 v23, v23, v36, v35
	v_div_fixup_f32 v40, v23, v22, v2
	v_fma_f32 v23, -v37, v38, 1.0
	v_fmac_f32_e32 v38, v23, v38
	v_div_scale_f32 v23, vcc, v5, v22, v5
	v_mul_f32_e32 v35, v23, v38
	v_fma_f32 v36, -v37, v35, v23
	v_fmac_f32_e32 v35, v36, v38
	v_div_scale_f32 v36, s[6:7], v22, v22, v4
	v_fma_f32 v23, -v37, v35, v23
	v_rcp_f32_e32 v37, v36
	v_div_fmas_f32 v23, v23, v38, v35
	v_div_fixup_f32 v43, v23, v22, v5
	v_fma_f32 v23, -v36, v37, 1.0
	v_fmac_f32_e32 v37, v23, v37
	v_div_scale_f32 v23, vcc, v4, v22, v4
	v_mul_f32_e32 v35, v23, v37
	v_fma_f32 v38, -v36, v35, v23
	v_fmac_f32_e32 v35, v38, v37
	v_fma_f32 v23, -v36, v35, v23
	v_div_fmas_f32 v23, v23, v37, v35
	v_div_fixup_f32 v42, v23, v22, v4
	v_pk_mul_f32 v[22:23], v[42:43], v[42:43]
	v_pk_mul_f32 v[36:37], v[40:41], v[40:41]
	s_nop 0
	v_pk_mov_b32 v[38:39], v[36:37], v[22:23] op_sel:[1,0]
	v_mov_b32_e32 v37, v23
	v_pk_add_f32 v[22:23], v[38:39], v[36:37]
	s_nop 0
	v_add_f32_e32 v22, v22, v23
	ds_bpermute_b32 v23, v25, v22
	s_waitcnt lgkmcnt(0)
	v_add_f32_e32 v35, v22, v23
	v_lshl_add_u64 v[22:23], v[14:15], 0, s[10:11]
	ds_bpermute_b32 v44, v26, v35
	s_waitcnt lgkmcnt(0)
	v_add_f32_e32 v35, v35, v44
	ds_bpermute_b32 v44, v27, v35
	s_waitcnt lgkmcnt(0)
	v_add_f32_e32 v35, v35, v44
	ds_bpermute_b32 v44, v28, v35
	s_waitcnt lgkmcnt(0)
	v_add_f32_e32 v35, v35, v44
	ds_bpermute_b32 v44, v29, v35
	s_waitcnt lgkmcnt(0)
	v_add_f32_e32 v35, v35, v44
	ds_bpermute_b32 v44, v30, v35
	s_waitcnt lgkmcnt(0)
	v_add_f32_e32 v35, v35, v44
	v_fmamk_f32 v35, v35, 0x3b800000, v10
	v_mul_f32_e32 v44, 0x4f800000, v35
	v_cmp_gt_f32_e32 vcc, s21, v35
	s_nop 1
	v_cndmask_b32_e32 v35, v35, v44, vcc
	v_sqrt_f32_e32 v44, v35
	s_nop 0
	v_add_u32_e32 v45, -1, v44
	v_fma_f32 v46, -v45, v44, v35
	v_cmp_ge_f32_e64 s[6:7], 0, v46
	v_add_u32_e32 v46, 1, v44
	s_nop 0
	v_cndmask_b32_e64 v45, v44, v45, s[6:7]
	v_fma_f32 v44, -v46, v44, v35
	v_cmp_lt_f32_e64 s[6:7], 0, v44
	s_nop 1
	v_cndmask_b32_e64 v44, v45, v46, s[6:7]
	v_mul_f32_e32 v45, 0x37800000, v44
	v_cndmask_b32_e32 v44, v44, v45, vcc
	v_cmp_class_f32_e32 vcc, v35, v31
	s_nop 1
	v_cndmask_b32_e32 v35, v44, v35, vcc
	v_div_scale_f32 v44, s[6:7], v35, v35, 1.0
	v_rcp_f32_e32 v45, v44
	s_ashr_i32 s6, s23, 2
	s_ashr_i32 s7, s6, 31
	s_lshl_b64 s[6:7], s[6:7], 12
	v_fma_f32 v46, -v44, v45, 1.0
	v_fmac_f32_e32 v45, v46, v45
	v_div_scale_f32 v46, vcc, 1.0, v35, 1.0
	v_mul_f32_e32 v47, v46, v45
	v_fma_f32 v48, -v44, v47, v46
	v_fmac_f32_e32 v47, v48, v45
	v_fma_f32 v44, -v44, v47, v46
	v_div_fmas_f32 v44, v44, v45, v47
	v_lshlrev_b32_e32 v45, 16, v12
	v_mul_f32_e32 v45, 0xbfb8aa3b, v45
	v_and_b32_e32 v46, 0xffff0000, v12
	v_exp_f32_e32 v45, v45
	v_mul_f32_e32 v46, 0xbfb8aa3b, v46
	v_exp_f32_e32 v47, v46
	v_div_fixup_f32 v44, v44, v35, 1.0
	v_add_f32_e32 v35, 1.0, v45
	v_rcp_f32_e32 v46, v35
	v_add_f32_e32 v35, 1.0, v47
	v_rcp_f32_e32 v47, v35
	v_lshlrev_b32_e32 v35, 16, v13
	v_pk_mul_f32 v[40:41], v[40:41], v[44:45] op_sel_hi:[1,0]
	v_mul_f32_e32 v35, 0xbfb8aa3b, v35
	v_and_b32_e32 v45, 0xffff0000, v13
	v_exp_f32_e32 v35, v35
	v_mul_f32_e32 v45, 0xbfb8aa3b, v45
	v_exp_f32_e32 v45, v45
	v_pk_mul_f32 v[36:37], v[240:241], v[40:41]
	v_add_f32_e32 v35, 1.0, v35
	v_rcp_f32_e32 v40, v35
	v_add_f32_e32 v35, 1.0, v45
	v_rcp_f32_e32 v41, v35
	v_pk_mul_f32 v[42:43], v[42:43], v[44:45] op_sel_hi:[1,0]
	s_add_u32 s6, s14, s6
	v_pk_mul_f32 v[38:39], v[242:243], v[42:43]
	s_addc_u32 s7, s15, s7
	s_lshl_b32 s10, s24, 1
	v_pk_mul_f32 v[36:37], v[46:47], v[36:37]
	v_pk_mul_f32 v[38:39], v[40:41], v[38:39]
	s_add_u32 s6, s6, s10
	v_cvt_pk_bf16_f32 v36, v36, v37
	v_cvt_pk_bf16_f32 v37, v38, v39
	s_addc_u32 s7, s7, 0
	s_andn2_b64 vcc, exec, s[0:1]
	global_store_dwordx2 v32, v[36:37], s[6:7] offset:2048
	s_cbranch_vccnz .LBB0_879
	s_add_i32 s0, s20, s23
	s_cmpk_gt_i32 s0, 0x7fff
	s_cbranch_scc1 .LBB0_878
	s_ashr_i32 s0, s0, 2
	s_ashr_i32 s1, s0, 31
	s_lshl_b64 s[6:7], s[0:1], 12
	v_lshl_add_u64 v[2:3], v[16:17], 0, s[6:7]
	s_add_u32 s6, s0, s17
	s_addc_u32 s7, s1, 0
	s_lshl_b64 s[6:7], s[6:7], 2
	s_add_u32 s24, s2, s6
	s_addc_u32 s25, s3, s7
	s_add_u32 s6, s12, s6
	s_addc_u32 s7, s13, s7
	s_lshl_b64 s[0:1], s[0:1], 11
	v_lshl_add_u64 v[12:13], v[18:19], 0, s[0:1]
	global_load_dword v1, v11, s[24:25]
	global_load_dword v24, v11, s[6:7]
	s_nop 0
	global_load_dwordx4 v[2:5], v[2:3], off
	s_nop 0
	global_load_dwordx2 v[12:13], v[12:13], off
	s_waitcnt vmcnt(5)
	s_branch .Lp5_gob
